# gate-ratio hook of the merged GEMM fetches its gate fragments 8 at a time; P1 int8 w_in pass 2 issues its tile loads before the counter poll
# speedup vs baseline: 1.0414x; 1.0124x over previous
; #define LAS __attribute__((address_space(3)))
; __device__ __forceinline__ void tr_load(const TrJob& j, f32x4 (&v)[16], int lane) {
;     if (j.lddst == 0) return;
;     const int kr = lane >> 4, n4 = (lane & 15) * 4;
; #pragma unroll
;     for (int q = 0; q < 16; ++q) v[q] = __builtin_nontemporal_load((const f32x4*)(j.src + (size_t)(4 * q + kr) * j.ldsrc + n4));
; }
; __device__ __forceinline__ void win_pass2(const Params& p, int l, int job, LAS float* scr, LAS float* colq, int lane) {
;     const int kb = job / 96, cb = job % 96; unsigned* ctl = (unsigned*)(p.ws + WS_CTL);
;     { unsigned spin = 0; while (__hip_atomic_load(ctl + CW_WCNT + l * 96 + cb, __ATOMIC_RELAXED, __HIP_MEMORY_SCOPE_AGENT) < 32u && ++spin < (1u << 22)) __builtin_amdgcn_s_sleep(2); }
;     { const float cs = fmaxf(__uint_as_float(__hip_atomic_load(ctl + CW_CMAX + l * INC + cb * 64 + lane, __ATOMIC_RELAXED, __HIP_MEMORY_SCOPE_AGENT)), 1e-30f);
;       colq[lane] = 127.0f / cs; if (kb == 0) ((float*)(p.ws + WS_SW))[(size_t)l * INC + cb * 64 + lane] = cs * (1.0f / 127.0f); }
;     unsigned char* wl = p.ws + WS_W + (size_t)l * WL_BYTES;
;     TrJob j; j.src = p.in[3] + (size_t)l * D * INC + (size_t)(kb * 64) * INC + cb * 64; j.ldsrc = INC; j.dst = (bf16*)(wl + WL_IG + ((size_t)kb * 2 * INC + cb * 64) * 64); j.lddst = -64; j.qmul = 0.f; j.i8 = 1;
;     f32x4 v[16]; tr_load(j, v, lane); tr_store(j, v, scr, lane, colq);
.LBB0_337:
	s_mul_hi_i32 s0, s18, 0x2aaaaaab
	s_lshr_b32 s1, s0, 31
	s_ashr_i32 s10, s0, 4
	s_add_i32 s10, s10, s1
	s_mul_i32 s0, s10, 0x60
	s_sub_i32 s0, s18, s0
	s_lshl_b32 s12, s0, 6
	s_ashr_i32 s13, s12, 31
	s_lshl_b64 s[12:13], s[12:13], 2
	s_lshl_b32 s14, s10, 6
	s_mul_i32 s15, s10, 0x180000
	v_readlane_b32 s8, v249, 13
	s_mul_hi_i32 s14, s14, 0x6000
	s_add_u32 s8, s8, s15
	v_readlane_b32 s15, v249, 22
	s_addc_u32 s9, s15, s14
	s_add_u32 s8, s8, s12
	s_addc_u32 s9, s9, s13
	v_mov_b32_e32 v108, v18
	v_mov_b32_e32 v109, v65
	v_lshl_add_u64 v[106:107], s[8:9], 0, v[64:65]
	v_lshl_add_u64 v[106:107], v[106:107], 0, v[108:109]
	s_mov_b64 s[12:13], 0x18000
	global_load_dwordx4 v[112:115], v[106:107], off nt
	v_lshl_add_u64 v[106:107], v[106:107], 0, s[12:13]
	global_load_dwordx4 v[116:119], v[106:107], off nt
	v_lshl_add_u64 v[106:107], v[106:107], 0, s[12:13]
	global_load_dwordx4 v[120:123], v[106:107], off nt
	v_lshl_add_u64 v[106:107], v[106:107], 0, s[12:13]
	global_load_dwordx4 v[124:127], v[106:107], off nt
	v_lshl_add_u64 v[106:107], v[106:107], 0, s[12:13]
	global_load_dwordx4 v[128:131], v[106:107], off nt
	v_lshl_add_u64 v[106:107], v[106:107], 0, s[12:13]
	global_load_dwordx4 v[132:135], v[106:107], off nt
	v_lshl_add_u64 v[106:107], v[106:107], 0, s[12:13]
	global_load_dwordx4 v[136:139], v[106:107], off nt
	v_lshl_add_u64 v[106:107], v[106:107], 0, s[12:13]
	global_load_dwordx4 v[140:143], v[106:107], off nt
	v_lshl_add_u64 v[106:107], v[106:107], 0, s[12:13]
	global_load_dwordx4 v[144:147], v[106:107], off nt
	v_lshl_add_u64 v[106:107], v[106:107], 0, s[12:13]
	global_load_dwordx4 v[148:151], v[106:107], off nt
	v_lshl_add_u64 v[106:107], v[106:107], 0, s[12:13]
	global_load_dwordx4 v[152:155], v[106:107], off nt
	v_lshl_add_u64 v[106:107], v[106:107], 0, s[12:13]
	global_load_dwordx4 v[156:159], v[106:107], off nt
	v_lshl_add_u64 v[106:107], v[106:107], 0, s[12:13]
	global_load_dwordx4 v[160:163], v[106:107], off nt
	v_lshl_add_u64 v[106:107], v[106:107], 0, s[12:13]
	global_load_dwordx4 v[164:167], v[106:107], off nt
	v_lshl_add_u64 v[106:107], v[106:107], 0, s[12:13]
	global_load_dwordx4 v[168:171], v[106:107], off nt
	v_lshl_add_u64 v[106:107], v[106:107], 0, s[12:13]
	global_load_dwordx4 v[172:175], v[106:107], off nt
	s_ashr_i32 s1, s0, 31
	s_lshl_b64 s[4:5], s[0:1], 2
	v_readlane_b32 s1, v249, 25
	s_add_u32 s4, s1, s4
	v_readlane_b32 s1, v249, 26
	s_addc_u32 s5, s1, s5
	global_load_dword v0, v65, s[4:5] sc1
	s_waitcnt vmcnt(0)
	v_cmp_lt_u32_e32 vcc, 31, v0
	s_cbranch_vccnz .LBB0_348
	s_mov_b32 s1, 0x3ffff8
	s_branch .LBB0_340

; #define LAS __attribute__((address_space(3)))
; __device__ __forceinline__ void tr_load(const TrJob& j, f32x4 (&v)[16], int lane) {
;     if (j.lddst == 0) return;
;     const int kr = lane >> 4, n4 = (lane & 15) * 4;
; #pragma unroll
;     for (int q = 0; q < 16; ++q) v[q] = __builtin_nontemporal_load((const f32x4*)(j.src + (size_t)(4 * q + kr) * j.ldsrc + n4));
; }
; __device__ __forceinline__ void tr_store(const TrJob& j, const f32x4 (&v)[16], LAS float* scr, int lane, const LAS float* colq = nullptr) {
;     if (j.lddst == 0) return;
;     const int kr = lane >> 4, n4 = (lane & 15) * 4;
; #pragma unroll
;     for (int q = 0; q < 16; ++q) { const int k = 4 * q + kr; *(LAS f32x4*)(scr + k * 64 + (n4 ^ (8 * (k >> 3)))) = v[q]; }
;     asm volatile("s_waitcnt lgkmcnt(0)" ::: "memory");
.LBB0_350:
	s_lshl_b32 s0, s10, 6
	s_mul_i32 s1, s10, 0x180000
	v_readlane_b32 s8, v249, 13
	s_mul_hi_i32 s0, s0, 0x6000
	s_add_u32 s8, s8, s1
	v_readlane_b32 s1, v249, 22
	s_addc_u32 s9, s1, s0
	s_lshl_b64 s[0:1], s[4:5], 2
	s_add_u32 s0, s8, s0
	s_addc_u32 s1, s9, s1
	v_lshl_add_u64 v[0:1], s[0:1], 0, v[64:65]
	v_mov_b32_e32 v19, v65
	v_lshl_add_u64 v[20:21], v[0:1], 0, v[18:19]
	s_mov_b32 s0, 0x18000
	v_add_co_u32_e32 v42, vcc, s0, v20
	s_mov_b32 s0, 0x30000
	s_nop 0
	v_addc_co_u32_e32 v43, vcc, 0, v21, vcc
	v_add_co_u32_e32 v46, vcc, s0, v20
	s_mov_b32 s0, 0x48000
	s_nop 0
	v_addc_co_u32_e32 v47, vcc, 0, v21, vcc
	v_add_co_u32_e32 v50, vcc, s0, v20
	s_mov_b32 s0, 0x60000
	s_nop 0
	v_addc_co_u32_e32 v51, vcc, 0, v21, vcc
	v_add_co_u32_e32 v54, vcc, s0, v20
	s_mov_b32 s0, 0x78000
	s_nop 0
	v_addc_co_u32_e32 v55, vcc, 0, v21, vcc
	v_add_co_u32_e32 v58, vcc, s0, v20
	s_mov_b32 s0, 0x90000
	s_nop 0
	v_addc_co_u32_e32 v59, vcc, 0, v21, vcc
	v_add_co_u32_e32 v62, vcc, s0, v20
	s_mov_b32 s0, 0xa8000
	s_nop 0
	v_addc_co_u32_e32 v63, vcc, 0, v21, vcc
	v_add_co_u32_e32 v70, vcc, s0, v20
	s_mov_b32 s0, 0xc0000
	s_nop 0
	v_addc_co_u32_e32 v71, vcc, 0, v21, vcc
	s_nop 0
	s_nop 0
	s_nop 0
	s_nop 0
	s_nop 0
	s_nop 0
	s_nop 0
	v_add_co_u32_e32 v62, vcc, s0, v20
	s_mov_b32 s0, 0xd8000
	s_nop 0
	v_addc_co_u32_e32 v63, vcc, 0, v21, vcc
	v_add_co_u32_e32 v78, vcc, s0, v20
	s_mov_b32 s0, 0xf0000
	s_nop 0
	v_addc_co_u32_e32 v79, vcc, 0, v21, vcc
	s_nop 0
	v_add_co_u32_e32 v62, vcc, s0, v20
	s_mov_b32 s0, 0x108000
	s_nop 0
	v_addc_co_u32_e32 v63, vcc, 0, v21, vcc
	v_add_co_u32_e32 v86, vcc, s0, v20
	s_mov_b32 s0, 0x120000
	s_nop 0
	v_addc_co_u32_e32 v87, vcc, 0, v21, vcc
	s_nop 0
	v_add_co_u32_e32 v62, vcc, s0, v20
	s_mov_b32 s0, 0x138000
	s_nop 0
	v_addc_co_u32_e32 v63, vcc, 0, v21, vcc
	v_add_co_u32_e32 v94, vcc, s0, v20
	s_mov_b32 s0, 0x150000
	s_nop 0
	v_addc_co_u32_e32 v95, vcc, 0, v21, vcc
	s_nop 0
	v_add_co_u32_e32 v62, vcc, s0, v20
	s_mov_b32 s0, 0x168000
	s_nop 0
	v_addc_co_u32_e32 v63, vcc, 0, v21, vcc
	v_add_co_u32_e32 v20, vcc, s0, v20
	v_add_u32_e32 v19, v23, v24
	s_nop 0
	v_addc_co_u32_e32 v21, vcc, 0, v21, vcc
	s_andn2_b64 vcc, exec, s[2:3]
	ds_write_b128 v19, v[112:115]
	ds_write_b128 v19, v[116:119] offset:1024
	ds_write_b128 v35, v[120:123] offset:2048
	ds_write_b128 v35, v[124:127] offset:3072
	ds_write_b128 v36, v[128:131] offset:4096
	ds_write_b128 v36, v[132:135] offset:5120
	ds_write_b128 v37, v[136:139] offset:6144
	ds_write_b128 v37, v[140:143] offset:7168
	ds_write_b128 v38, v[144:147] offset:8192
	ds_write_b128 v38, v[148:151] offset:9216
	ds_write_b128 v39, v[152:155] offset:10240
	ds_write_b128 v39, v[156:159] offset:11264
	ds_write_b128 v40, v[160:163] offset:12288
	ds_write_b128 v40, v[164:167] offset:13312
	ds_write_b128 v41, v[168:171] offset:14336
	ds_write_b128 v41, v[172:175] offset:15360
	s_waitcnt lgkmcnt(0)
	v_cndmask_b32_e64 v0, 0, 1, s[2:3]
	v_mov_b32_e32 v19, 0
	v_cmp_ne_u32_e64 s[0:1], 1, v0
	v_mov_b32_e32 v3, 0
	s_cbranch_vccnz .LBB0_352
	ds_read_b32 v3, v27

; __device__ __forceinline__ float bflo(unsigned w) { return __uint_as_float(w << 16); }
; __device__ __forceinline__ float bfhi(unsigned w) { return __uint_as_float(w & 0xffff0000u); }
;     __device__ __forceinline__ void mid(f32x4 (&acc)[2][2][4][2], const Unit& u, int seg, int wr, int wc, int fr, int fq) const {
;         int opq = 0; asm volatile("" : "+v"(opq));
;         const int row0 = u.orow + wr * 64 + fr + opq, colw = wc * 32 + 8 * fq;
; #pragma unroll
;         for (int ai = 0; ai < 2; ++ai)
; #pragma unroll
;             for (int m = 0; m < 4; ++m) { const bf16* gp = GATE + (size_t)(row0 + ai * HALF + m * 16) * INC + (size_t)(seg - 1) * D + u.pn * BM + colw;
; #pragma unroll
;                 for (int bj = 0; bj < 2; ++bj) { const u32x4 a = *(const u32x4*)(gp + bj * HALF), b = *(const u32x4*)(gp + D + bj * HALF);
;                     f32x4 r0, r1;
;                     r0[0] = bflo(a.x) * __builtin_amdgcn_rcpf(fmaxf(bflo(b.x), 1e-30f)); r0[1] = bfhi(a.x) * __builtin_amdgcn_rcpf(fmaxf(bfhi(b.x), 1e-30f));
;                     r0[2] = bflo(a.y) * __builtin_amdgcn_rcpf(fmaxf(bflo(b.y), 1e-30f)); r0[3] = bfhi(a.y) * __builtin_amdgcn_rcpf(fmaxf(bfhi(b.y), 1e-30f));
;                     r1[0] = bflo(a.z) * __builtin_amdgcn_rcpf(fmaxf(bflo(b.z), 1e-30f)); r1[1] = bfhi(a.z) * __builtin_amdgcn_rcpf(fmaxf(bfhi(b.z), 1e-30f));
;                     r1[2] = bflo(a.w) * __builtin_amdgcn_rcpf(fmaxf(bflo(b.w), 1e-30f)); r1[3] = bfhi(a.w) * __builtin_amdgcn_rcpf(fmaxf(bfhi(b.w), 1e-30f));
;                     acc[ai][bj][m][0] *= r0; acc[ai][bj][m][1] *= r1; }
;                 asm volatile("" ::: "memory"); }
;     }
.LBB0_704:
	s_andn2_b64 vcc, exec, s[0:1]
	s_cbranch_vccnz .LBB0_706
	v_readlane_b32 s16, v251, 3
	s_lshr_b32 s0, s50, 3
	v_mov_b32_e32 v0, v65
	v_readlane_b32 s17, v251, 4
	s_add_i32 s88, s0, -1
	v_add_u32_e32 v8, v0, v212
	v_mov_b64_e32 v[4:5], s[16:17]
	s_lshl_b64 s[0:1], s[88:89], 12
	v_mad_i64_i32 v[0:1], s[16:17], v8, s97, v[4:5]
	v_lshl_add_u64 v[0:1], v[0:1], 0, s[0:1]
	s_lshl_b64 s[16:17], s[12:13], 1
	v_lshl_add_u64 v[0:1], v[0:1], 0, s[16:17]
	v_lshlrev_b32_e32 v64, 1, v206
	v_lshl_add_u64 v[2:3], v[0:1], 0, v[64:65]
	s_movk_i32 s19, 0x1000
	v_add_u32_e32 v52, 0, v8
	v_mad_i64_i32 v[52:53], s[20:21], v52, s97, v[4:5]
	v_lshl_add_u64 v[52:53], v[52:53], 0, s[0:1]
	v_lshl_add_u64 v[52:53], v[52:53], 0, s[16:17]
	v_lshl_add_u64 v[52:53], v[52:53], 0, v[64:65]
	v_add_co_u32_e32 v54, vcc, s19, v52
	s_nop 1
	v_addc_co_u32_e32 v55, vcc, 0, v53, vcc
	global_load_dwordx4 v[20:23], v[52:53], off
	global_load_dwordx4 v[24:27], v[54:55], off
	global_load_dwordx4 v[28:31], v[52:53], off offset:256
	global_load_dwordx4 v[32:35], v[54:55], off offset:256
	v_add_u32_e32 v52, 16, v8
	v_mad_i64_i32 v[52:53], s[20:21], v52, s97, v[4:5]
	v_lshl_add_u64 v[52:53], v[52:53], 0, s[0:1]
	v_lshl_add_u64 v[52:53], v[52:53], 0, s[16:17]
	v_lshl_add_u64 v[52:53], v[52:53], 0, v[64:65]
	v_add_co_u32_e32 v54, vcc, s19, v52
	s_nop 1
	v_addc_co_u32_e32 v55, vcc, 0, v53, vcc
	global_load_dwordx4 v[36:39], v[52:53], off
	global_load_dwordx4 v[40:43], v[54:55], off
	global_load_dwordx4 v[44:47], v[52:53], off offset:256
	global_load_dwordx4 v[48:51], v[54:55], off offset:256
	v_add_co_u32_e32 v0, vcc, s19, v2
	s_waitcnt vmcnt(7)
	v_mov_b64_e32 v[10:11], v[20:21]
	v_mov_b64_e32 v[12:13], v[22:23]
	s_nop 0
	v_addc_co_u32_e32 v1, vcc, 0, v3, vcc
	s_waitcnt vmcnt(6)
	v_mov_b64_e32 v[14:15], v[24:25]
	v_mov_b64_e32 v[16:17], v[26:27]
	v_lshlrev_b32_e32 v18, 16, v10
	v_and_b32_e32 v19, 0xffff0000, v10
	v_lshlrev_b32_e32 v10, 16, v11
	v_lshlrev_b32_e32 v9, 16, v15
	v_max_f32_e32 v9, v9, v9
	v_max_f32_e32 v9, 0xda24260, v9
	v_lshlrev_b32_e32 v6, 16, v14
	v_and_b32_e32 v7, 0xffff0000, v14
	v_rcp_f32_e32 v14, v9
	v_and_b32_e32 v9, 0xffff0000, v15
	v_max_f32_e32 v9, v9, v9
	v_max_f32_e32 v9, 0xda24260, v9
	v_rcp_f32_e32 v15, v9
	v_lshlrev_b32_e32 v9, 16, v16
	v_max_f32_e32 v9, v9, v9
	v_and_b32_e32 v11, 0xffff0000, v11
	v_max_f32_e32 v9, 0xda24260, v9
	v_pk_mul_f32 v[10:11], v[14:15], v[10:11]
	v_rcp_f32_e32 v14, v9
	v_and_b32_e32 v9, 0xffff0000, v16
	v_max_f32_e32 v9, v9, v9
	v_max_f32_e32 v9, 0xda24260, v9
	v_rcp_f32_e32 v15, v9
	v_lshlrev_b32_e32 v9, 16, v17
	v_max_f32_e32 v9, v9, v9
	v_max_f32_e32 v9, 0xda24260, v9
	v_max_f32_e32 v6, v6, v6
	v_max_f32_e32 v7, v7, v7
	v_rcp_f32_e32 v16, v9
	v_and_b32_e32 v9, 0xffff0000, v17
	v_max_f32_e32 v6, 0xda24260, v6
	v_max_f32_e32 v7, 0xda24260, v7
	v_max_f32_e32 v9, v9, v9
	v_rcp_f32_e32 v6, v6
	v_rcp_f32_e32 v7, v7
	v_max_f32_e32 v9, 0xda24260, v9
	v_rcp_f32_e32 v17, v9
	v_pk_mul_f32 v[192:193], v[192:193], v[10:11]
	v_pk_mul_f32 v[6:7], v[6:7], v[18:19]
	v_lshlrev_b32_e32 v18, 16, v12
	v_and_b32_e32 v19, 0xffff0000, v12
	v_lshlrev_b32_e32 v12, 16, v13
	v_and_b32_e32 v13, 0xffff0000, v13
	v_pk_mul_f32 v[12:13], v[16:17], v[12:13]
	v_pk_mul_f32 v[190:191], v[190:191], v[6:7]
	v_pk_mul_f32 v[188:189], v[188:189], v[12:13]
	s_waitcnt vmcnt(5)
	v_mov_b64_e32 v[10:11], v[28:29]
	v_mov_b64_e32 v[12:13], v[30:31]
	s_nop 0
	s_waitcnt vmcnt(4)
	v_mov_b64_e32 v[0:1], v[32:33]
	v_mov_b64_e32 v[2:3], v[34:35]
	v_pk_mul_f32 v[14:15], v[14:15], v[18:19]
	v_lshlrev_b32_e32 v6, 16, v0
	v_and_b32_e32 v0, 0xffff0000, v0
	v_max_f32_e32 v0, v0, v0
	v_max_f32_e32 v0, 0xda24260, v0
	v_rcp_f32_e32 v7, v0
	v_lshlrev_b32_e32 v0, 16, v1
	v_and_b32_e32 v1, 0xffff0000, v1
	v_max_f32_e32 v0, v0, v0
	v_max_f32_e32 v1, v1, v1
	v_max_f32_e32 v0, 0xda24260, v0
	v_max_f32_e32 v1, 0xda24260, v1
	v_rcp_f32_e32 v0, v0
	v_rcp_f32_e32 v1, v1
	v_lshlrev_b32_e32 v9, 16, v2
	v_and_b32_e32 v2, 0xffff0000, v2
	v_max_f32_e32 v6, v6, v6
	v_max_f32_e32 v2, v2, v2
	v_pk_mul_f32 v[186:187], v[186:187], v[14:15]
	v_max_f32_e32 v6, 0xda24260, v6
	v_lshlrev_b32_e32 v14, 16, v10
	v_and_b32_e32 v15, 0xffff0000, v10
	v_lshlrev_b32_e32 v10, 16, v11
	v_and_b32_e32 v11, 0xffff0000, v11
	v_max_f32_e32 v9, v9, v9
	v_max_f32_e32 v2, 0xda24260, v2
	v_rcp_f32_e32 v6, v6
	v_pk_mul_f32 v[0:1], v[0:1], v[10:11]
	v_max_f32_e32 v9, 0xda24260, v9
	v_rcp_f32_e32 v11, v2
	v_lshlrev_b32_e32 v2, 16, v3
	v_and_b32_e32 v3, 0xffff0000, v3
	v_rcp_f32_e32 v10, v9
	v_max_f32_e32 v2, v2, v2
	v_max_f32_e32 v3, v3, v3
	v_pk_mul_f32 v[184:185], v[184:185], v[0:1]
	v_add_u32_e32 v0, 16, v8
	v_max_f32_e32 v2, 0xda24260, v2
	v_max_f32_e32 v3, 0xda24260, v3
	v_mad_i64_i32 v[0:1], s[20:21], v0, s97, v[4:5]
	v_rcp_f32_e32 v2, v2
	v_rcp_f32_e32 v3, v3
	v_lshl_add_u64 v[0:1], v[0:1], 0, s[0:1]
	v_pk_mul_f32 v[6:7], v[6:7], v[14:15]
	v_lshlrev_b32_e32 v14, 16, v12
	v_and_b32_e32 v15, 0xffff0000, v12
	v_lshl_add_u64 v[0:1], v[0:1], 0, s[16:17]
	v_pk_mul_f32 v[10:11], v[10:11], v[14:15]
	v_lshl_add_u64 v[14:15], v[0:1], 0, v[64:65]
	v_lshlrev_b32_e32 v12, 16, v13
	v_and_b32_e32 v13, 0xffff0000, v13
	v_pk_mul_f32 v[182:183], v[182:183], v[6:7]
	v_add_co_u32_e32 v6, vcc, s19, v14
	v_pk_mul_f32 v[2:3], v[2:3], v[12:13]
	s_nop 0
	v_addc_co_u32_e32 v7, vcc, 0, v15, vcc
	v_pk_mul_f32 v[180:181], v[180:181], v[2:3]
	v_pk_mul_f32 v[178:179], v[178:179], v[10:11]
	s_waitcnt vmcnt(3)
	v_mov_b64_e32 v[0:1], v[36:37]
	v_mov_b64_e32 v[2:3], v[38:39]
	s_waitcnt vmcnt(2)
; __device__ __forceinline__ float bflo(unsigned w) { return __uint_as_float(w << 16); }
; __device__ __forceinline__ float bfhi(unsigned w) { return __uint_as_float(w & 0xffff0000u); }
;     __device__ __forceinline__ void mid(f32x4 (&acc)[2][2][4][2], const Unit& u, int seg, int wr, int wc, int fr, int fq) const {
;         int opq = 0; asm volatile("" : "+v"(opq));
;         const int row0 = u.orow + wr * 64 + fr + opq, colw = wc * 32 + 8 * fq;
; #pragma unroll
;         for (int ai = 0; ai < 2; ++ai)
; #pragma unroll
;             for (int m = 0; m < 4; ++m) { const bf16* gp = GATE + (size_t)(row0 + ai * HALF + m * 16) * INC + (size_t)(seg - 1) * D + u.pn * BM + colw;
; #pragma unroll
;                 for (int bj = 0; bj < 2; ++bj) { const u32x4 a = *(const u32x4*)(gp + bj * HALF), b = *(const u32x4*)(gp + D + bj * HALF);
;                     f32x4 r0, r1;
;                     r0[0] = bflo(a.x) * __builtin_amdgcn_rcpf(fmaxf(bflo(b.x), 1e-30f)); r0[1] = bfhi(a.x) * __builtin_amdgcn_rcpf(fmaxf(bfhi(b.x), 1e-30f));
;                     r0[2] = bflo(a.y) * __builtin_amdgcn_rcpf(fmaxf(bflo(b.y), 1e-30f)); r0[3] = bfhi(a.y) * __builtin_amdgcn_rcpf(fmaxf(bfhi(b.y), 1e-30f));
;                     r1[0] = bflo(a.z) * __builtin_amdgcn_rcpf(fmaxf(bflo(b.z), 1e-30f)); r1[1] = bfhi(a.z) * __builtin_amdgcn_rcpf(fmaxf(bfhi(b.z), 1e-30f));
;                     r1[2] = bflo(a.w) * __builtin_amdgcn_rcpf(fmaxf(bflo(b.w), 1e-30f)); r1[3] = bfhi(a.w) * __builtin_amdgcn_rcpf(fmaxf(bfhi(b.w), 1e-30f));
;                     acc[ai][bj][m][0] *= r0; acc[ai][bj][m][1] *= r1; }
;                 asm volatile("" ::: "memory"); }
;     }
	v_mov_b64_e32 v[10:11], v[40:41]
	v_mov_b64_e32 v[12:13], v[42:43]
	v_lshlrev_b32_e32 v18, 16, v0
	v_lshlrev_b32_e32 v9, 16, v10
	v_max_f32_e32 v9, v9, v9
	v_max_f32_e32 v9, 0xda24260, v9
	v_rcp_f32_e32 v16, v9
	v_and_b32_e32 v9, 0xffff0000, v10
	v_and_b32_e32 v19, 0xffff0000, v0
	v_lshlrev_b32_e32 v0, 16, v11
	v_max_f32_e32 v9, v9, v9
	v_max_f32_e32 v0, v0, v0
	v_max_f32_e32 v9, 0xda24260, v9
	v_max_f32_e32 v0, 0xda24260, v0
	v_rcp_f32_e32 v17, v9
	v_rcp_f32_e32 v10, v0
	v_and_b32_e32 v0, 0xffff0000, v11
	v_max_f32_e32 v0, v0, v0
	v_max_f32_e32 v0, 0xda24260, v0
	v_rcp_f32_e32 v11, v0
	v_pk_mul_f32 v[16:17], v[16:17], v[18:19]
	v_lshlrev_b32_e32 v9, 16, v12
	v_lshlrev_b32_e32 v18, 16, v2
	v_and_b32_e32 v19, 0xffff0000, v2
	v_lshlrev_b32_e32 v2, 16, v13
	v_max_f32_e32 v9, v9, v9
	v_max_f32_e32 v2, v2, v2
	v_lshlrev_b32_e32 v0, 16, v1
	v_and_b32_e32 v1, 0xffff0000, v1
	v_max_f32_e32 v9, 0xda24260, v9
	v_max_f32_e32 v2, 0xda24260, v2
	v_pk_mul_f32 v[0:1], v[10:11], v[0:1]
	v_rcp_f32_e32 v10, v9
	v_and_b32_e32 v9, 0xffff0000, v12
	v_rcp_f32_e32 v12, v2
	v_and_b32_e32 v2, 0xffff0000, v13
	v_max_f32_e32 v9, v9, v9
	v_max_f32_e32 v2, v2, v2
	v_max_f32_e32 v9, 0xda24260, v9
	v_max_f32_e32 v2, 0xda24260, v2
	v_rcp_f32_e32 v11, v9
	v_rcp_f32_e32 v13, v2
	v_lshlrev_b32_e32 v2, 16, v3
	v_and_b32_e32 v3, 0xffff0000, v3
	v_pk_mul_f32 v[10:11], v[10:11], v[18:19]
	v_pk_mul_f32 v[2:3], v[12:13], v[2:3]
	v_pk_mul_f32 v[176:177], v[176:177], v[0:1]
	v_pk_mul_f32 v[172:173], v[172:173], v[2:3]
	v_pk_mul_f32 v[170:171], v[170:171], v[10:11]
	s_waitcnt vmcnt(1)
	v_mov_b64_e32 v[0:1], v[44:45]
	v_mov_b64_e32 v[2:3], v[46:47]
	s_waitcnt vmcnt(0)
	v_mov_b64_e32 v[10:11], v[48:49]
	v_mov_b64_e32 v[12:13], v[50:51]
	v_pk_mul_f32 v[174:175], v[174:175], v[16:17]
	v_lshlrev_b32_e32 v14, 16, v0
	v_and_b32_e32 v15, 0xffff0000, v0
	v_lshlrev_b32_e32 v0, 16, v11
	v_max_f32_e32 v0, v0, v0
	v_lshlrev_b32_e32 v6, 16, v10
	v_and_b32_e32 v7, 0xffff0000, v10
	v_max_f32_e32 v0, 0xda24260, v0
	v_max_f32_e32 v6, v6, v6
	v_max_f32_e32 v7, v7, v7
	v_rcp_f32_e32 v10, v0
	v_and_b32_e32 v0, 0xffff0000, v11
	v_max_f32_e32 v6, 0xda24260, v6
	v_max_f32_e32 v7, 0xda24260, v7
	v_max_f32_e32 v0, v0, v0
	v_rcp_f32_e32 v6, v6
	v_rcp_f32_e32 v7, v7
	v_max_f32_e32 v0, 0xda24260, v0
	v_rcp_f32_e32 v11, v0
	v_lshlrev_b32_e32 v9, 16, v12
	v_max_f32_e32 v9, v9, v9
	v_pk_mul_f32 v[6:7], v[6:7], v[14:15]
	v_lshlrev_b32_e32 v0, 16, v1
	v_and_b32_e32 v1, 0xffff0000, v1
	v_max_f32_e32 v9, 0xda24260, v9
	v_lshlrev_b32_e32 v14, 16, v2
	v_and_b32_e32 v15, 0xffff0000, v2
	v_lshlrev_b32_e32 v2, 16, v13
	v_pk_mul_f32 v[0:1], v[10:11], v[0:1]
	v_rcp_f32_e32 v10, v9
	v_and_b32_e32 v9, 0xffff0000, v12
	v_max_f32_e32 v2, v2, v2
	v_max_f32_e32 v9, v9, v9
	v_max_f32_e32 v2, 0xda24260, v2
	v_max_f32_e32 v9, 0xda24260, v9
	v_rcp_f32_e32 v12, v2
	v_and_b32_e32 v2, 0xffff0000, v13
	v_rcp_f32_e32 v11, v9
	v_max_f32_e32 v2, v2, v2
	v_pk_mul_f32 v[168:169], v[168:169], v[0:1]
	v_add_u32_e32 v52, 32, v8
	v_mad_i64_i32 v[52:53], s[20:21], v52, s97, v[4:5]
	v_lshl_add_u64 v[52:53], v[52:53], 0, s[0:1]
	v_lshl_add_u64 v[52:53], v[52:53], 0, s[16:17]
	v_lshl_add_u64 v[52:53], v[52:53], 0, v[64:65]
	v_add_co_u32_e32 v54, vcc, s19, v52
	s_nop 1
	v_addc_co_u32_e32 v55, vcc, 0, v53, vcc
	global_load_dwordx4 v[20:23], v[52:53], off
	global_load_dwordx4 v[24:27], v[54:55], off
	global_load_dwordx4 v[28:31], v[52:53], off offset:256
	global_load_dwordx4 v[32:35], v[54:55], off offset:256
	v_add_u32_e32 v52, 48, v8
	v_mad_i64_i32 v[52:53], s[20:21], v52, s97, v[4:5]
	v_lshl_add_u64 v[52:53], v[52:53], 0, s[0:1]
	v_lshl_add_u64 v[52:53], v[52:53], 0, s[16:17]
	v_lshl_add_u64 v[52:53], v[52:53], 0, v[64:65]
	v_add_co_u32_e32 v54, vcc, s19, v52
	s_nop 1
	v_addc_co_u32_e32 v55, vcc, 0, v53, vcc
	global_load_dwordx4 v[36:39], v[52:53], off
	global_load_dwordx4 v[40:43], v[54:55], off
	global_load_dwordx4 v[44:47], v[52:53], off offset:256
	global_load_dwordx4 v[48:51], v[54:55], off offset:256
	v_add_u32_e32 v0, 32, v8
	v_max_f32_e32 v2, 0xda24260, v2
	v_mad_i64_i32 v[0:1], s[20:21], v0, s97, v[4:5]
	v_rcp_f32_e32 v13, v2
	v_lshl_add_u64 v[0:1], v[0:1], 0, s[0:1]
	v_lshl_add_u64 v[0:1], v[0:1], 0, s[16:17]
	v_pk_mul_f32 v[10:11], v[10:11], v[14:15]
	v_lshl_add_u64 v[14:15], v[0:1], 0, v[64:65]
	v_lshlrev_b32_e32 v2, 16, v3
	v_and_b32_e32 v3, 0xffff0000, v3
	v_pk_mul_f32 v[166:167], v[166:167], v[6:7]
	v_add_co_u32_e32 v6, vcc, s19, v14
	v_pk_mul_f32 v[2:3], v[12:13], v[2:3]
	s_nop 0
	v_addc_co_u32_e32 v7, vcc, 0, v15, vcc
	v_pk_mul_f32 v[164:165], v[164:165], v[2:3]
	v_pk_mul_f32 v[162:163], v[162:163], v[10:11]
	s_waitcnt vmcnt(7)
	v_mov_b64_e32 v[0:1], v[20:21]
	v_mov_b64_e32 v[2:3], v[22:23]
	s_waitcnt vmcnt(6)
	v_mov_b64_e32 v[10:11], v[24:25]
	v_mov_b64_e32 v[12:13], v[26:27]
	v_lshlrev_b32_e32 v18, 16, v0
	v_lshlrev_b32_e32 v9, 16, v10
	v_max_f32_e32 v9, v9, v9
	v_max_f32_e32 v9, 0xda24260, v9
	v_rcp_f32_e32 v16, v9
	v_and_b32_e32 v9, 0xffff0000, v10
	v_and_b32_e32 v19, 0xffff0000, v0
	v_lshlrev_b32_e32 v0, 16, v11
	v_max_f32_e32 v9, v9, v9
	v_max_f32_e32 v0, v0, v0
	v_max_f32_e32 v9, 0xda24260, v9
	v_max_f32_e32 v0, 0xda24260, v0
	v_rcp_f32_e32 v17, v9
	v_rcp_f32_e32 v10, v0
	v_and_b32_e32 v0, 0xffff0000, v11
	v_max_f32_e32 v0, v0, v0
	v_max_f32_e32 v0, 0xda24260, v0
	v_rcp_f32_e32 v11, v0
	v_pk_mul_f32 v[16:17], v[16:17], v[18:19]
	v_lshlrev_b32_e32 v9, 16, v12
	v_lshlrev_b32_e32 v18, 16, v2
	v_and_b32_e32 v19, 0xffff0000, v2
	v_lshlrev_b32_e32 v2, 16, v13
	v_max_f32_e32 v9, v9, v9
	v_max_f32_e32 v2, v2, v2
	v_lshlrev_b32_e32 v0, 16, v1
	v_and_b32_e32 v1, 0xffff0000, v1
	v_max_f32_e32 v9, 0xda24260, v9
	v_max_f32_e32 v2, 0xda24260, v2
	v_pk_mul_f32 v[0:1], v[10:11], v[0:1]
	v_rcp_f32_e32 v10, v9
	v_and_b32_e32 v9, 0xffff0000, v12
	v_rcp_f32_e32 v12, v2
	v_and_b32_e32 v2, 0xffff0000, v13
	v_max_f32_e32 v9, v9, v9
	v_max_f32_e32 v2, v2, v2
	v_max_f32_e32 v9, 0xda24260, v9
	v_max_f32_e32 v2, 0xda24260, v2
	v_rcp_f32_e32 v11, v9
	v_rcp_f32_e32 v13, v2
	v_lshlrev_b32_e32 v2, 16, v3
	v_and_b32_e32 v3, 0xffff0000, v3
	v_pk_mul_f32 v[10:11], v[10:11], v[18:19]
	v_pk_mul_f32 v[2:3], v[12:13], v[2:3]
	v_pk_mul_f32 v[160:161], v[160:161], v[0:1]
	v_pk_mul_f32 v[156:157], v[156:157], v[2:3]
	v_pk_mul_f32 v[154:155], v[154:155], v[10:11]
	s_waitcnt vmcnt(5)
; __device__ __forceinline__ float bflo(unsigned w) { return __uint_as_float(w << 16); }
; __device__ __forceinline__ float bfhi(unsigned w) { return __uint_as_float(w & 0xffff0000u); }
;     __device__ __forceinline__ void mid(f32x4 (&acc)[2][2][4][2], const Unit& u, int seg, int wr, int wc, int fr, int fq) const {
;         int opq = 0; asm volatile("" : "+v"(opq));
;         const int row0 = u.orow + wr * 64 + fr + opq, colw = wc * 32 + 8 * fq;
; #pragma unroll
;         for (int ai = 0; ai < 2; ++ai)
; #pragma unroll
;             for (int m = 0; m < 4; ++m) { const bf16* gp = GATE + (size_t)(row0 + ai * HALF + m * 16) * INC + (size_t)(seg - 1) * D + u.pn * BM + colw;
; #pragma unroll
;                 for (int bj = 0; bj < 2; ++bj) { const u32x4 a = *(const u32x4*)(gp + bj * HALF), b = *(const u32x4*)(gp + D + bj * HALF);
;                     f32x4 r0, r1;
;                     r0[0] = bflo(a.x) * __builtin_amdgcn_rcpf(fmaxf(bflo(b.x), 1e-30f)); r0[1] = bfhi(a.x) * __builtin_amdgcn_rcpf(fmaxf(bfhi(b.x), 1e-30f));
;                     r0[2] = bflo(a.y) * __builtin_amdgcn_rcpf(fmaxf(bflo(b.y), 1e-30f)); r0[3] = bfhi(a.y) * __builtin_amdgcn_rcpf(fmaxf(bfhi(b.y), 1e-30f));
;                     r1[0] = bflo(a.z) * __builtin_amdgcn_rcpf(fmaxf(bflo(b.z), 1e-30f)); r1[1] = bfhi(a.z) * __builtin_amdgcn_rcpf(fmaxf(bfhi(b.z), 1e-30f));
;                     r1[2] = bflo(a.w) * __builtin_amdgcn_rcpf(fmaxf(bflo(b.w), 1e-30f)); r1[3] = bfhi(a.w) * __builtin_amdgcn_rcpf(fmaxf(bfhi(b.w), 1e-30f));
;                     acc[ai][bj][m][0] *= r0; acc[ai][bj][m][1] *= r1; }
;                 asm volatile("" ::: "memory"); }
;     }
	v_mov_b64_e32 v[0:1], v[28:29]
	v_mov_b64_e32 v[2:3], v[30:31]
	s_waitcnt vmcnt(4)
	v_mov_b64_e32 v[10:11], v[32:33]
	v_mov_b64_e32 v[12:13], v[34:35]
	v_pk_mul_f32 v[158:159], v[158:159], v[16:17]
	v_lshlrev_b32_e32 v14, 16, v0
	v_and_b32_e32 v15, 0xffff0000, v0
	v_lshlrev_b32_e32 v0, 16, v11
	v_max_f32_e32 v0, v0, v0
	v_lshlrev_b32_e32 v6, 16, v10
	v_and_b32_e32 v7, 0xffff0000, v10
	v_max_f32_e32 v0, 0xda24260, v0
	v_max_f32_e32 v6, v6, v6
	v_max_f32_e32 v7, v7, v7
	v_rcp_f32_e32 v10, v0
	v_and_b32_e32 v0, 0xffff0000, v11
	v_max_f32_e32 v6, 0xda24260, v6
	v_max_f32_e32 v7, 0xda24260, v7
	v_max_f32_e32 v0, v0, v0
	v_rcp_f32_e32 v6, v6
	v_rcp_f32_e32 v7, v7
	v_max_f32_e32 v0, 0xda24260, v0
	v_rcp_f32_e32 v11, v0
	v_lshlrev_b32_e32 v9, 16, v12
	v_max_f32_e32 v9, v9, v9
	v_pk_mul_f32 v[6:7], v[6:7], v[14:15]
	v_lshlrev_b32_e32 v0, 16, v1
	v_and_b32_e32 v1, 0xffff0000, v1
	v_max_f32_e32 v9, 0xda24260, v9
	v_lshlrev_b32_e32 v14, 16, v2
	v_and_b32_e32 v15, 0xffff0000, v2
	v_lshlrev_b32_e32 v2, 16, v13
	v_pk_mul_f32 v[0:1], v[10:11], v[0:1]
	v_rcp_f32_e32 v10, v9
	v_and_b32_e32 v9, 0xffff0000, v12
	v_max_f32_e32 v2, v2, v2
	v_max_f32_e32 v9, v9, v9
	v_max_f32_e32 v2, 0xda24260, v2
	v_max_f32_e32 v9, 0xda24260, v9
	v_rcp_f32_e32 v12, v2
	v_and_b32_e32 v2, 0xffff0000, v13
	v_rcp_f32_e32 v11, v9
	v_max_f32_e32 v2, v2, v2
	v_pk_mul_f32 v[152:153], v[152:153], v[0:1]
	v_add_u32_e32 v0, 48, v8
	v_max_f32_e32 v2, 0xda24260, v2
	v_mad_i64_i32 v[0:1], s[20:21], v0, s97, v[4:5]
	v_rcp_f32_e32 v13, v2
	v_lshl_add_u64 v[0:1], v[0:1], 0, s[0:1]
	v_lshl_add_u64 v[0:1], v[0:1], 0, s[16:17]
	v_pk_mul_f32 v[10:11], v[10:11], v[14:15]
	v_lshl_add_u64 v[14:15], v[0:1], 0, v[64:65]
	v_lshlrev_b32_e32 v2, 16, v3
	v_and_b32_e32 v3, 0xffff0000, v3
	v_pk_mul_f32 v[150:151], v[150:151], v[6:7]
	v_add_co_u32_e32 v6, vcc, s19, v14
	v_pk_mul_f32 v[2:3], v[12:13], v[2:3]
	s_nop 0
	v_addc_co_u32_e32 v7, vcc, 0, v15, vcc
	v_pk_mul_f32 v[148:149], v[148:149], v[2:3]
	v_pk_mul_f32 v[146:147], v[146:147], v[10:11]
	s_waitcnt vmcnt(3)
	v_mov_b64_e32 v[0:1], v[36:37]
	v_mov_b64_e32 v[2:3], v[38:39]
	s_waitcnt vmcnt(2)
	v_mov_b64_e32 v[10:11], v[40:41]
	v_mov_b64_e32 v[12:13], v[42:43]
	v_lshlrev_b32_e32 v18, 16, v0
	v_lshlrev_b32_e32 v9, 16, v10
	v_max_f32_e32 v9, v9, v9
	v_max_f32_e32 v9, 0xda24260, v9
	v_rcp_f32_e32 v16, v9
	v_and_b32_e32 v9, 0xffff0000, v10
	v_and_b32_e32 v19, 0xffff0000, v0
	v_lshlrev_b32_e32 v0, 16, v11
	v_max_f32_e32 v9, v9, v9
	v_max_f32_e32 v0, v0, v0
	v_max_f32_e32 v9, 0xda24260, v9
	v_max_f32_e32 v0, 0xda24260, v0
	v_rcp_f32_e32 v17, v9
	v_rcp_f32_e32 v10, v0
	v_and_b32_e32 v0, 0xffff0000, v11
	v_max_f32_e32 v0, v0, v0
	v_max_f32_e32 v0, 0xda24260, v0
	v_rcp_f32_e32 v11, v0
	v_pk_mul_f32 v[16:17], v[16:17], v[18:19]
	v_lshlrev_b32_e32 v9, 16, v12
	v_lshlrev_b32_e32 v18, 16, v2
	v_and_b32_e32 v19, 0xffff0000, v2
	v_lshlrev_b32_e32 v2, 16, v13
	v_max_f32_e32 v9, v9, v9
	v_max_f32_e32 v2, v2, v2
	v_lshlrev_b32_e32 v0, 16, v1
	v_and_b32_e32 v1, 0xffff0000, v1
	v_max_f32_e32 v9, 0xda24260, v9
	v_max_f32_e32 v2, 0xda24260, v2
	v_pk_mul_f32 v[0:1], v[10:11], v[0:1]
	v_rcp_f32_e32 v10, v9
	v_and_b32_e32 v9, 0xffff0000, v12
	v_rcp_f32_e32 v12, v2
	v_and_b32_e32 v2, 0xffff0000, v13
	v_max_f32_e32 v9, v9, v9
	v_max_f32_e32 v2, v2, v2
	v_max_f32_e32 v9, 0xda24260, v9
	v_max_f32_e32 v2, 0xda24260, v2
	v_rcp_f32_e32 v11, v9
	v_rcp_f32_e32 v13, v2
	v_lshlrev_b32_e32 v2, 16, v3
	v_and_b32_e32 v3, 0xffff0000, v3
	v_pk_mul_f32 v[10:11], v[10:11], v[18:19]
	v_pk_mul_f32 v[2:3], v[12:13], v[2:3]
	v_pk_mul_f32 v[144:145], v[144:145], v[0:1]
	v_pk_mul_f32 v[140:141], v[140:141], v[2:3]
	v_pk_mul_f32 v[138:139], v[138:139], v[10:11]
	s_waitcnt vmcnt(1)
	v_mov_b64_e32 v[0:1], v[44:45]
	v_mov_b64_e32 v[2:3], v[46:47]
	s_waitcnt vmcnt(0)
	v_mov_b64_e32 v[10:11], v[48:49]
	v_mov_b64_e32 v[12:13], v[50:51]
	v_pk_mul_f32 v[142:143], v[142:143], v[16:17]
	v_lshlrev_b32_e32 v14, 16, v0
	v_and_b32_e32 v15, 0xffff0000, v0
	v_lshlrev_b32_e32 v0, 16, v11
	v_max_f32_e32 v0, v0, v0
	v_lshlrev_b32_e32 v6, 16, v10
	v_and_b32_e32 v7, 0xffff0000, v10
	v_max_f32_e32 v0, 0xda24260, v0
	v_max_f32_e32 v6, v6, v6
	v_max_f32_e32 v7, v7, v7
	v_rcp_f32_e32 v10, v0
	v_and_b32_e32 v0, 0xffff0000, v11
	v_max_f32_e32 v6, 0xda24260, v6
	v_max_f32_e32 v7, 0xda24260, v7
	v_max_f32_e32 v0, v0, v0
	v_rcp_f32_e32 v6, v6
	v_rcp_f32_e32 v7, v7
	v_max_f32_e32 v0, 0xda24260, v0
	v_rcp_f32_e32 v11, v0
	v_lshlrev_b32_e32 v9, 16, v12
	v_max_f32_e32 v9, v9, v9
	v_pk_mul_f32 v[6:7], v[6:7], v[14:15]
	v_lshlrev_b32_e32 v0, 16, v1
	v_and_b32_e32 v1, 0xffff0000, v1
	v_max_f32_e32 v9, 0xda24260, v9
	v_lshlrev_b32_e32 v14, 16, v2
	v_and_b32_e32 v15, 0xffff0000, v2
	v_lshlrev_b32_e32 v2, 16, v13
	v_pk_mul_f32 v[0:1], v[10:11], v[0:1]
	v_rcp_f32_e32 v10, v9
	v_and_b32_e32 v9, 0xffff0000, v12
	v_max_f32_e32 v2, v2, v2
	v_max_f32_e32 v9, v9, v9
	v_max_f32_e32 v2, 0xda24260, v2
	v_max_f32_e32 v9, 0xda24260, v9
	v_rcp_f32_e32 v12, v2
	v_and_b32_e32 v2, 0xffff0000, v13
	v_rcp_f32_e32 v11, v9
	v_max_f32_e32 v2, v2, v2
	v_pk_mul_f32 v[136:137], v[136:137], v[0:1]
	v_add_u32_e32 v52, 0x80, v8
	v_mad_i64_i32 v[52:53], s[20:21], v52, s97, v[4:5]
	v_lshl_add_u64 v[52:53], v[52:53], 0, s[0:1]
	v_lshl_add_u64 v[52:53], v[52:53], 0, s[16:17]
	v_lshl_add_u64 v[52:53], v[52:53], 0, v[64:65]
	v_add_co_u32_e32 v54, vcc, s19, v52
	s_nop 1
	v_addc_co_u32_e32 v55, vcc, 0, v53, vcc
	global_load_dwordx4 v[20:23], v[52:53], off
	global_load_dwordx4 v[24:27], v[54:55], off
	global_load_dwordx4 v[28:31], v[52:53], off offset:256
	global_load_dwordx4 v[32:35], v[54:55], off offset:256
	v_add_u32_e32 v52, 0x90, v8
	v_mad_i64_i32 v[52:53], s[20:21], v52, s97, v[4:5]
	v_lshl_add_u64 v[52:53], v[52:53], 0, s[0:1]
	v_lshl_add_u64 v[52:53], v[52:53], 0, s[16:17]
	v_lshl_add_u64 v[52:53], v[52:53], 0, v[64:65]
	v_add_co_u32_e32 v54, vcc, s19, v52
	s_nop 1
	v_addc_co_u32_e32 v55, vcc, 0, v53, vcc
	global_load_dwordx4 v[36:39], v[52:53], off
	global_load_dwordx4 v[40:43], v[54:55], off
	global_load_dwordx4 v[44:47], v[52:53], off offset:256
	global_load_dwordx4 v[48:51], v[54:55], off offset:256
	v_add_u32_e32 v0, 0x80, v8
	v_max_f32_e32 v2, 0xda24260, v2
	v_mad_i64_i32 v[0:1], s[20:21], v0, s97, v[4:5]
	v_rcp_f32_e32 v13, v2
	v_lshl_add_u64 v[0:1], v[0:1], 0, s[0:1]
	v_lshl_add_u64 v[0:1], v[0:1], 0, s[16:17]
	v_pk_mul_f32 v[10:11], v[10:11], v[14:15]
	v_lshl_add_u64 v[14:15], v[0:1], 0, v[64:65]
	v_lshlrev_b32_e32 v2, 16, v3
	v_and_b32_e32 v3, 0xffff0000, v3
	v_pk_mul_f32 v[134:135], v[134:135], v[6:7]
	v_add_co_u32_e32 v6, vcc, s19, v14
	v_pk_mul_f32 v[2:3], v[12:13], v[2:3]
	s_nop 0
	v_addc_co_u32_e32 v7, vcc, 0, v15, vcc
	v_pk_mul_f32 v[132:133], v[132:133], v[2:3]
	v_pk_mul_f32 v[130:131], v[130:131], v[10:11]
	s_waitcnt vmcnt(7)
; __device__ __forceinline__ float bflo(unsigned w) { return __uint_as_float(w << 16); }
; __device__ __forceinline__ float bfhi(unsigned w) { return __uint_as_float(w & 0xffff0000u); }
;     __device__ __forceinline__ void mid(f32x4 (&acc)[2][2][4][2], const Unit& u, int seg, int wr, int wc, int fr, int fq) const {
;     ...
;             for (int m = 0; m < 4; ++m) { const bf16* gp = GATE + (size_t)(row0 + ai * HALF + m * 16) * INC + (size_t)(seg - 1) * D + u.pn * BM + colw;
; #pragma unroll
;                 for (int bj = 0; bj < 2; ++bj) { const u32x4 a = *(const u32x4*)(gp + bj * HALF), b = *(const u32x4*)(gp + D + bj * HALF);
;                     f32x4 r0, r1;
;                     r0[0] = bflo(a.x) * __builtin_amdgcn_rcpf(fmaxf(bflo(b.x), 1e-30f)); r0[1] = bfhi(a.x) * __builtin_amdgcn_rcpf(fmaxf(bfhi(b.x), 1e-30f));
;                     r0[2] = bflo(a.y) * __builtin_amdgcn_rcpf(fmaxf(bflo(b.y), 1e-30f)); r0[3] = bfhi(a.y) * __builtin_amdgcn_rcpf(fmaxf(bfhi(b.y), 1e-30f));
;                     r1[0] = bflo(a.z) * __builtin_amdgcn_rcpf(fmaxf(bflo(b.z), 1e-30f)); r1[1] = bfhi(a.z) * __builtin_amdgcn_rcpf(fmaxf(bfhi(b.z), 1e-30f));
;                     r1[2] = bflo(a.w) * __builtin_amdgcn_rcpf(fmaxf(bflo(b.w), 1e-30f)); r1[3] = bfhi(a.w) * __builtin_amdgcn_rcpf(fmaxf(bfhi(b.w), 1e-30f));
;                     acc[ai][bj][m][0] *= r0; acc[ai][bj][m][1] *= r1; }
;                 asm volatile("" ::: "memory"); }
	v_mov_b64_e32 v[0:1], v[20:21]
	v_mov_b64_e32 v[2:3], v[22:23]
	s_waitcnt vmcnt(6)
	v_mov_b64_e32 v[10:11], v[24:25]
	v_mov_b64_e32 v[12:13], v[26:27]
	v_lshlrev_b32_e32 v18, 16, v0
	v_lshlrev_b32_e32 v9, 16, v10
	v_max_f32_e32 v9, v9, v9
	v_max_f32_e32 v9, 0xda24260, v9
	v_rcp_f32_e32 v16, v9
	v_and_b32_e32 v9, 0xffff0000, v10
	v_and_b32_e32 v19, 0xffff0000, v0
	v_lshlrev_b32_e32 v0, 16, v11
	v_max_f32_e32 v9, v9, v9
	v_max_f32_e32 v0, v0, v0
	v_max_f32_e32 v9, 0xda24260, v9
	v_max_f32_e32 v0, 0xda24260, v0
	v_rcp_f32_e32 v17, v9
	v_rcp_f32_e32 v10, v0
	v_and_b32_e32 v0, 0xffff0000, v11
	v_max_f32_e32 v0, v0, v0
	v_max_f32_e32 v0, 0xda24260, v0
	v_rcp_f32_e32 v11, v0
	v_pk_mul_f32 v[16:17], v[16:17], v[18:19]
	v_lshlrev_b32_e32 v9, 16, v12
	v_lshlrev_b32_e32 v18, 16, v2
	v_and_b32_e32 v19, 0xffff0000, v2
	v_lshlrev_b32_e32 v2, 16, v13
	v_max_f32_e32 v9, v9, v9
	v_max_f32_e32 v2, v2, v2
	v_lshlrev_b32_e32 v0, 16, v1
	v_and_b32_e32 v1, 0xffff0000, v1
	v_max_f32_e32 v9, 0xda24260, v9
	v_max_f32_e32 v2, 0xda24260, v2
	v_pk_mul_f32 v[0:1], v[10:11], v[0:1]
	v_rcp_f32_e32 v10, v9
	v_and_b32_e32 v9, 0xffff0000, v12
	v_rcp_f32_e32 v12, v2
	v_and_b32_e32 v2, 0xffff0000, v13
	v_max_f32_e32 v9, v9, v9
	v_max_f32_e32 v2, v2, v2
	v_max_f32_e32 v9, 0xda24260, v9
	v_max_f32_e32 v2, 0xda24260, v2
	v_rcp_f32_e32 v11, v9
	v_rcp_f32_e32 v13, v2
	v_lshlrev_b32_e32 v2, 16, v3
	v_and_b32_e32 v3, 0xffff0000, v3
	v_pk_mul_f32 v[10:11], v[10:11], v[18:19]
	v_pk_mul_f32 v[2:3], v[12:13], v[2:3]
	v_pk_mul_f32 v[128:129], v[128:129], v[0:1]
	v_pk_mul_f32 v[124:125], v[124:125], v[2:3]
	v_pk_mul_f32 v[122:123], v[122:123], v[10:11]
	s_waitcnt vmcnt(5)
	v_mov_b64_e32 v[0:1], v[28:29]
	v_mov_b64_e32 v[2:3], v[30:31]
	s_waitcnt vmcnt(4)
	v_mov_b64_e32 v[10:11], v[32:33]
	v_mov_b64_e32 v[12:13], v[34:35]
	v_pk_mul_f32 v[126:127], v[126:127], v[16:17]
	v_lshlrev_b32_e32 v14, 16, v0
	v_and_b32_e32 v15, 0xffff0000, v0
	v_lshlrev_b32_e32 v0, 16, v11
	v_max_f32_e32 v0, v0, v0
	v_lshlrev_b32_e32 v6, 16, v10
	v_and_b32_e32 v7, 0xffff0000, v10
	v_max_f32_e32 v0, 0xda24260, v0
	v_max_f32_e32 v6, v6, v6
	v_max_f32_e32 v7, v7, v7
	v_rcp_f32_e32 v10, v0
	v_and_b32_e32 v0, 0xffff0000, v11
	v_max_f32_e32 v6, 0xda24260, v6
	v_max_f32_e32 v7, 0xda24260, v7
	v_max_f32_e32 v0, v0, v0
	v_rcp_f32_e32 v6, v6
	v_rcp_f32_e32 v7, v7
	v_max_f32_e32 v0, 0xda24260, v0
	v_rcp_f32_e32 v11, v0
	v_lshlrev_b32_e32 v9, 16, v12
	v_max_f32_e32 v9, v9, v9
	v_pk_mul_f32 v[6:7], v[6:7], v[14:15]
	v_lshlrev_b32_e32 v0, 16, v1
	v_and_b32_e32 v1, 0xffff0000, v1
	v_max_f32_e32 v9, 0xda24260, v9
	v_lshlrev_b32_e32 v14, 16, v2
	v_and_b32_e32 v15, 0xffff0000, v2
	v_lshlrev_b32_e32 v2, 16, v13
	v_pk_mul_f32 v[0:1], v[10:11], v[0:1]
	v_rcp_f32_e32 v10, v9
	v_and_b32_e32 v9, 0xffff0000, v12
	v_max_f32_e32 v2, v2, v2
	v_max_f32_e32 v9, v9, v9
	v_max_f32_e32 v2, 0xda24260, v2
	v_max_f32_e32 v9, 0xda24260, v9
	v_rcp_f32_e32 v12, v2
	v_and_b32_e32 v2, 0xffff0000, v13
	v_rcp_f32_e32 v11, v9
	v_max_f32_e32 v2, v2, v2
	v_pk_mul_f32 v[120:121], v[120:121], v[0:1]
	v_add_u32_e32 v0, 0x90, v8
	v_max_f32_e32 v2, 0xda24260, v2
	v_mad_i64_i32 v[0:1], s[20:21], v0, s97, v[4:5]
	v_rcp_f32_e32 v13, v2
	v_lshl_add_u64 v[0:1], v[0:1], 0, s[0:1]
	v_lshl_add_u64 v[0:1], v[0:1], 0, s[16:17]
	v_pk_mul_f32 v[10:11], v[10:11], v[14:15]
	v_lshl_add_u64 v[14:15], v[0:1], 0, v[64:65]
	v_lshlrev_b32_e32 v2, 16, v3
	v_and_b32_e32 v3, 0xffff0000, v3
	v_pk_mul_f32 v[118:119], v[118:119], v[6:7]
	v_add_co_u32_e32 v6, vcc, s19, v14
	v_pk_mul_f32 v[2:3], v[12:13], v[2:3]
	s_nop 0
	v_addc_co_u32_e32 v7, vcc, 0, v15, vcc
	v_pk_mul_f32 v[116:117], v[116:117], v[2:3]
	v_pk_mul_f32 v[114:115], v[114:115], v[10:11]
	s_waitcnt vmcnt(3)
	v_mov_b64_e32 v[0:1], v[36:37]
	v_mov_b64_e32 v[2:3], v[38:39]
	s_waitcnt vmcnt(2)
	v_mov_b64_e32 v[10:11], v[40:41]
	v_mov_b64_e32 v[12:13], v[42:43]
	v_lshlrev_b32_e32 v18, 16, v0
	v_lshlrev_b32_e32 v9, 16, v10
	v_max_f32_e32 v9, v9, v9
	v_max_f32_e32 v9, 0xda24260, v9
	v_rcp_f32_e32 v16, v9
	v_and_b32_e32 v9, 0xffff0000, v10
	v_and_b32_e32 v19, 0xffff0000, v0
	v_lshlrev_b32_e32 v0, 16, v11
	v_max_f32_e32 v9, v9, v9
	v_max_f32_e32 v0, v0, v0
	v_max_f32_e32 v9, 0xda24260, v9
	v_max_f32_e32 v0, 0xda24260, v0
	v_rcp_f32_e32 v17, v9
	v_rcp_f32_e32 v10, v0
	v_and_b32_e32 v0, 0xffff0000, v11
	v_max_f32_e32 v0, v0, v0
	v_max_f32_e32 v0, 0xda24260, v0
	v_rcp_f32_e32 v11, v0
	v_pk_mul_f32 v[16:17], v[16:17], v[18:19]
	v_lshlrev_b32_e32 v9, 16, v12
	v_lshlrev_b32_e32 v18, 16, v2
	v_and_b32_e32 v19, 0xffff0000, v2
	v_lshlrev_b32_e32 v2, 16, v13
	v_max_f32_e32 v9, v9, v9
	v_max_f32_e32 v2, v2, v2
	v_lshlrev_b32_e32 v0, 16, v1
	v_and_b32_e32 v1, 0xffff0000, v1
	v_max_f32_e32 v9, 0xda24260, v9
	v_max_f32_e32 v2, 0xda24260, v2
	v_pk_mul_f32 v[0:1], v[10:11], v[0:1]
	v_rcp_f32_e32 v10, v9
	v_and_b32_e32 v9, 0xffff0000, v12
	v_rcp_f32_e32 v12, v2
	v_and_b32_e32 v2, 0xffff0000, v13
	v_max_f32_e32 v9, v9, v9
	v_max_f32_e32 v2, v2, v2
	v_max_f32_e32 v9, 0xda24260, v9
	v_max_f32_e32 v2, 0xda24260, v2
	v_rcp_f32_e32 v11, v9
	v_rcp_f32_e32 v13, v2
	v_lshlrev_b32_e32 v2, 16, v3
	v_and_b32_e32 v3, 0xffff0000, v3
	v_pk_mul_f32 v[10:11], v[10:11], v[18:19]
	v_pk_mul_f32 v[2:3], v[12:13], v[2:3]
	v_pk_mul_f32 v[112:113], v[112:113], v[0:1]
	v_pk_mul_f32 v[108:109], v[108:109], v[2:3]
	v_pk_mul_f32 v[106:107], v[106:107], v[10:11]
	s_waitcnt vmcnt(1)
	v_mov_b64_e32 v[0:1], v[44:45]
	v_mov_b64_e32 v[2:3], v[46:47]
	s_waitcnt vmcnt(0)
; __device__ __forceinline__ float bflo(unsigned w) { return __uint_as_float(w << 16); }
; __device__ __forceinline__ float bfhi(unsigned w) { return __uint_as_float(w & 0xffff0000u); }
;     __device__ __forceinline__ void mid(f32x4 (&acc)[2][2][4][2], const Unit& u, int seg, int wr, int wc, int fr, int fq) const {
;     ...
;             for (int m = 0; m < 4; ++m) { const bf16* gp = GATE + (size_t)(row0 + ai * HALF + m * 16) * INC + (size_t)(seg - 1) * D + u.pn * BM + colw;
; #pragma unroll
;                 for (int bj = 0; bj < 2; ++bj) { const u32x4 a = *(const u32x4*)(gp + bj * HALF), b = *(const u32x4*)(gp + D + bj * HALF);
;                     f32x4 r0, r1;
;                     r0[0] = bflo(a.x) * __builtin_amdgcn_rcpf(fmaxf(bflo(b.x), 1e-30f)); r0[1] = bfhi(a.x) * __builtin_amdgcn_rcpf(fmaxf(bfhi(b.x), 1e-30f));
;                     r0[2] = bflo(a.y) * __builtin_amdgcn_rcpf(fmaxf(bflo(b.y), 1e-30f)); r0[3] = bfhi(a.y) * __builtin_amdgcn_rcpf(fmaxf(bfhi(b.y), 1e-30f));
;                     r1[0] = bflo(a.z) * __builtin_amdgcn_rcpf(fmaxf(bflo(b.z), 1e-30f)); r1[1] = bfhi(a.z) * __builtin_amdgcn_rcpf(fmaxf(bfhi(b.z), 1e-30f));
;                     r1[2] = bflo(a.w) * __builtin_amdgcn_rcpf(fmaxf(bflo(b.w), 1e-30f)); r1[3] = bfhi(a.w) * __builtin_amdgcn_rcpf(fmaxf(bfhi(b.w), 1e-30f));
;                     acc[ai][bj][m][0] *= r0; acc[ai][bj][m][1] *= r1; }
;                 asm volatile("" ::: "memory"); }
	v_mov_b64_e32 v[10:11], v[48:49]
	v_mov_b64_e32 v[12:13], v[50:51]
	v_pk_mul_f32 v[110:111], v[110:111], v[16:17]
	v_lshlrev_b32_e32 v14, 16, v0
	v_and_b32_e32 v15, 0xffff0000, v0
	v_lshlrev_b32_e32 v0, 16, v11
	v_max_f32_e32 v0, v0, v0
	v_lshlrev_b32_e32 v6, 16, v10
	v_and_b32_e32 v7, 0xffff0000, v10
	v_max_f32_e32 v0, 0xda24260, v0
	v_max_f32_e32 v6, v6, v6
	v_max_f32_e32 v7, v7, v7
	v_rcp_f32_e32 v10, v0
	v_and_b32_e32 v0, 0xffff0000, v11
	v_max_f32_e32 v6, 0xda24260, v6
	v_max_f32_e32 v7, 0xda24260, v7
	v_max_f32_e32 v0, v0, v0
	v_rcp_f32_e32 v6, v6
	v_rcp_f32_e32 v7, v7
	v_max_f32_e32 v0, 0xda24260, v0
	v_rcp_f32_e32 v11, v0
	v_lshlrev_b32_e32 v9, 16, v12
	v_max_f32_e32 v9, v9, v9
	v_pk_mul_f32 v[6:7], v[6:7], v[14:15]
	v_lshlrev_b32_e32 v0, 16, v1
	v_and_b32_e32 v1, 0xffff0000, v1
	v_max_f32_e32 v9, 0xda24260, v9
	v_lshlrev_b32_e32 v14, 16, v2
	v_and_b32_e32 v15, 0xffff0000, v2
	v_lshlrev_b32_e32 v2, 16, v13
	v_pk_mul_f32 v[0:1], v[10:11], v[0:1]
	v_rcp_f32_e32 v10, v9
	v_and_b32_e32 v9, 0xffff0000, v12
	v_max_f32_e32 v2, v2, v2
	v_max_f32_e32 v9, v9, v9
	v_max_f32_e32 v2, 0xda24260, v2
	v_max_f32_e32 v9, 0xda24260, v9
	v_rcp_f32_e32 v12, v2
	v_and_b32_e32 v2, 0xffff0000, v13
	v_rcp_f32_e32 v11, v9
	v_max_f32_e32 v2, v2, v2
	v_pk_mul_f32 v[104:105], v[104:105], v[0:1]
	v_add_u32_e32 v52, 0xa0, v8
	v_mad_i64_i32 v[52:53], s[20:21], v52, s97, v[4:5]
	v_lshl_add_u64 v[52:53], v[52:53], 0, s[0:1]
	v_lshl_add_u64 v[52:53], v[52:53], 0, s[16:17]
	v_lshl_add_u64 v[52:53], v[52:53], 0, v[64:65]
	v_add_co_u32_e32 v54, vcc, s19, v52
	s_nop 1
	v_addc_co_u32_e32 v55, vcc, 0, v53, vcc
	global_load_dwordx4 v[20:23], v[52:53], off
	global_load_dwordx4 v[24:27], v[54:55], off
	global_load_dwordx4 v[28:31], v[52:53], off offset:256
	global_load_dwordx4 v[32:35], v[54:55], off offset:256
	v_add_u32_e32 v52, 0xb0, v8
	v_mad_i64_i32 v[52:53], s[20:21], v52, s97, v[4:5]
	v_lshl_add_u64 v[52:53], v[52:53], 0, s[0:1]
	v_lshl_add_u64 v[52:53], v[52:53], 0, s[16:17]
	v_lshl_add_u64 v[52:53], v[52:53], 0, v[64:65]
	v_add_co_u32_e32 v54, vcc, s19, v52
	s_nop 1
	v_addc_co_u32_e32 v55, vcc, 0, v53, vcc
	global_load_dwordx4 v[36:39], v[52:53], off
	global_load_dwordx4 v[40:43], v[54:55], off
	global_load_dwordx4 v[44:47], v[52:53], off offset:256
	global_load_dwordx4 v[48:51], v[54:55], off offset:256
	v_add_u32_e32 v0, 0xa0, v8
	v_max_f32_e32 v2, 0xda24260, v2
	v_mad_i64_i32 v[0:1], s[20:21], v0, s97, v[4:5]
	v_rcp_f32_e32 v13, v2
	v_lshl_add_u64 v[0:1], v[0:1], 0, s[0:1]
	v_lshl_add_u64 v[0:1], v[0:1], 0, s[16:17]
	v_pk_mul_f32 v[10:11], v[10:11], v[14:15]
	v_lshl_add_u64 v[14:15], v[0:1], 0, v[64:65]
	v_lshlrev_b32_e32 v2, 16, v3
	v_and_b32_e32 v3, 0xffff0000, v3
	v_pk_mul_f32 v[102:103], v[102:103], v[6:7]
	v_add_co_u32_e32 v6, vcc, s19, v14
	v_pk_mul_f32 v[2:3], v[12:13], v[2:3]
	s_nop 0
	v_addc_co_u32_e32 v7, vcc, 0, v15, vcc
	v_pk_mul_f32 v[100:101], v[100:101], v[2:3]
	v_pk_mul_f32 v[98:99], v[98:99], v[10:11]
	s_waitcnt vmcnt(7)
	v_mov_b64_e32 v[0:1], v[20:21]
	v_mov_b64_e32 v[2:3], v[22:23]
	s_waitcnt vmcnt(6)
	v_mov_b64_e32 v[10:11], v[24:25]
	v_mov_b64_e32 v[12:13], v[26:27]
	v_lshlrev_b32_e32 v18, 16, v0
	v_lshlrev_b32_e32 v9, 16, v10
	v_max_f32_e32 v9, v9, v9
	v_max_f32_e32 v9, 0xda24260, v9
	v_rcp_f32_e32 v16, v9
	v_and_b32_e32 v9, 0xffff0000, v10
	v_and_b32_e32 v19, 0xffff0000, v0
	v_lshlrev_b32_e32 v0, 16, v11
	v_max_f32_e32 v9, v9, v9
	v_max_f32_e32 v0, v0, v0
	v_max_f32_e32 v9, 0xda24260, v9
	v_max_f32_e32 v0, 0xda24260, v0
	v_rcp_f32_e32 v17, v9
	v_rcp_f32_e32 v10, v0
	v_and_b32_e32 v0, 0xffff0000, v11
	v_max_f32_e32 v0, v0, v0
	v_max_f32_e32 v0, 0xda24260, v0
	v_rcp_f32_e32 v11, v0
	v_pk_mul_f32 v[16:17], v[16:17], v[18:19]
	v_lshlrev_b32_e32 v9, 16, v12
	v_lshlrev_b32_e32 v18, 16, v2
	v_and_b32_e32 v19, 0xffff0000, v2
	v_lshlrev_b32_e32 v2, 16, v13
	v_max_f32_e32 v9, v9, v9
	v_max_f32_e32 v2, v2, v2
	v_lshlrev_b32_e32 v0, 16, v1
	v_and_b32_e32 v1, 0xffff0000, v1
	v_max_f32_e32 v9, 0xda24260, v9
	v_max_f32_e32 v2, 0xda24260, v2
	v_pk_mul_f32 v[0:1], v[10:11], v[0:1]
	v_rcp_f32_e32 v10, v9
	v_and_b32_e32 v9, 0xffff0000, v12
	v_rcp_f32_e32 v12, v2
	v_and_b32_e32 v2, 0xffff0000, v13
	v_max_f32_e32 v9, v9, v9
	v_max_f32_e32 v2, v2, v2
	v_max_f32_e32 v9, 0xda24260, v9
	v_max_f32_e32 v2, 0xda24260, v2
	v_rcp_f32_e32 v11, v9
	v_rcp_f32_e32 v13, v2
	v_lshlrev_b32_e32 v2, 16, v3
	v_and_b32_e32 v3, 0xffff0000, v3
	v_pk_mul_f32 v[10:11], v[10:11], v[18:19]
	v_pk_mul_f32 v[2:3], v[12:13], v[2:3]
	v_pk_mul_f32 v[96:97], v[96:97], v[0:1]
	v_pk_mul_f32 v[92:93], v[92:93], v[2:3]
	v_pk_mul_f32 v[90:91], v[90:91], v[10:11]
	s_waitcnt vmcnt(5)
	v_mov_b64_e32 v[0:1], v[28:29]
	v_mov_b64_e32 v[2:3], v[30:31]
	s_waitcnt vmcnt(4)
; __device__ __forceinline__ float bflo(unsigned w) { return __uint_as_float(w << 16); }
; __device__ __forceinline__ float bfhi(unsigned w) { return __uint_as_float(w & 0xffff0000u); }
;     __device__ __forceinline__ void mid(f32x4 (&acc)[2][2][4][2], const Unit& u, int seg, int wr, int wc, int fr, int fq) const {
;     ...
;             for (int m = 0; m < 4; ++m) { const bf16* gp = GATE + (size_t)(row0 + ai * HALF + m * 16) * INC + (size_t)(seg - 1) * D + u.pn * BM + colw;
; #pragma unroll
;                 for (int bj = 0; bj < 2; ++bj) { const u32x4 a = *(const u32x4*)(gp + bj * HALF), b = *(const u32x4*)(gp + D + bj * HALF);
;                     f32x4 r0, r1;
;                     r0[0] = bflo(a.x) * __builtin_amdgcn_rcpf(fmaxf(bflo(b.x), 1e-30f)); r0[1] = bfhi(a.x) * __builtin_amdgcn_rcpf(fmaxf(bfhi(b.x), 1e-30f));
;                     r0[2] = bflo(a.y) * __builtin_amdgcn_rcpf(fmaxf(bflo(b.y), 1e-30f)); r0[3] = bfhi(a.y) * __builtin_amdgcn_rcpf(fmaxf(bfhi(b.y), 1e-30f));
;                     r1[0] = bflo(a.z) * __builtin_amdgcn_rcpf(fmaxf(bflo(b.z), 1e-30f)); r1[1] = bfhi(a.z) * __builtin_amdgcn_rcpf(fmaxf(bfhi(b.z), 1e-30f));
;                     r1[2] = bflo(a.w) * __builtin_amdgcn_rcpf(fmaxf(bflo(b.w), 1e-30f)); r1[3] = bfhi(a.w) * __builtin_amdgcn_rcpf(fmaxf(bfhi(b.w), 1e-30f));
;                     acc[ai][bj][m][0] *= r0; acc[ai][bj][m][1] *= r1; }
;                 asm volatile("" ::: "memory"); }
	v_mov_b64_e32 v[10:11], v[32:33]
	v_mov_b64_e32 v[12:13], v[34:35]
	v_pk_mul_f32 v[94:95], v[94:95], v[16:17]
	v_lshlrev_b32_e32 v14, 16, v0
	v_and_b32_e32 v15, 0xffff0000, v0
	v_lshlrev_b32_e32 v0, 16, v11
	v_max_f32_e32 v0, v0, v0
	v_max_f32_e32 v0, 0xda24260, v0
	v_lshlrev_b32_e32 v6, 16, v10
	v_and_b32_e32 v7, 0xffff0000, v10
	v_rcp_f32_e32 v10, v0
	v_and_b32_e32 v0, 0xffff0000, v11
	v_max_f32_e32 v6, v6, v6
	v_max_f32_e32 v7, v7, v7
	v_max_f32_e32 v0, v0, v0
	v_max_f32_e32 v6, 0xda24260, v6
	v_max_f32_e32 v7, 0xda24260, v7
	v_max_f32_e32 v0, 0xda24260, v0
	v_rcp_f32_e32 v6, v6
	v_rcp_f32_e32 v7, v7
	v_rcp_f32_e32 v11, v0
	v_lshlrev_b32_e32 v9, 16, v12
	v_max_f32_e32 v9, v9, v9
	v_lshlrev_b32_e32 v0, 16, v1
	v_and_b32_e32 v1, 0xffff0000, v1
	v_max_f32_e32 v9, 0xda24260, v9
	v_pk_mul_f32 v[6:7], v[6:7], v[14:15]
	v_pk_mul_f32 v[0:1], v[10:11], v[0:1]
	v_rcp_f32_e32 v10, v9
	v_and_b32_e32 v9, 0xffff0000, v12
	v_lshlrev_b32_e32 v14, 16, v2
	v_and_b32_e32 v15, 0xffff0000, v2
	v_lshlrev_b32_e32 v2, 16, v13
	v_max_f32_e32 v9, v9, v9
	v_max_f32_e32 v2, v2, v2
	v_max_f32_e32 v9, 0xda24260, v9
	v_max_f32_e32 v2, 0xda24260, v2
	v_rcp_f32_e32 v11, v9
	v_rcp_f32_e32 v12, v2
	v_and_b32_e32 v2, 0xffff0000, v13
	v_max_f32_e32 v2, v2, v2
	v_pk_mul_f32 v[88:89], v[88:89], v[0:1]
	v_add_u32_e32 v0, 0xb0, v8
	v_max_f32_e32 v2, 0xda24260, v2
	v_mad_i64_i32 v[0:1], s[20:21], v0, s97, v[4:5]
	v_rcp_f32_e32 v13, v2
	v_lshl_add_u64 v[0:1], v[0:1], 0, s[0:1]
	v_pk_mul_f32 v[10:11], v[10:11], v[14:15]
	v_lshl_add_u64 v[0:1], v[0:1], 0, s[16:17]
	v_pk_mul_f32 v[82:83], v[82:83], v[10:11]
	v_lshl_add_u64 v[10:11], v[0:1], 0, v[64:65]
	v_lshlrev_b32_e32 v2, 16, v3
	v_and_b32_e32 v3, 0xffff0000, v3
	v_add_co_u32_e32 v4, vcc, s19, v10
	v_pk_mul_f32 v[2:3], v[12:13], v[2:3]
	s_nop 0
	v_addc_co_u32_e32 v5, vcc, 0, v11, vcc
	v_pk_mul_f32 v[86:87], v[86:87], v[6:7]
	v_pk_mul_f32 v[84:85], v[84:85], v[2:3]
	s_waitcnt vmcnt(3)
	v_mov_b64_e32 v[0:1], v[36:37]
	v_mov_b64_e32 v[2:3], v[38:39]
	s_waitcnt vmcnt(2)
	v_mov_b64_e32 v[6:7], v[40:41]
	v_mov_b64_e32 v[8:9], v[42:43]
	v_lshlrev_b32_e32 v14, 16, v0
	v_lshlrev_b32_e32 v12, 16, v6
	v_and_b32_e32 v6, 0xffff0000, v6
	v_and_b32_e32 v15, 0xffff0000, v0
	v_lshlrev_b32_e32 v0, 16, v7
	v_max_f32_e32 v12, v12, v12
	v_max_f32_e32 v6, v6, v6
	v_max_f32_e32 v0, v0, v0
	v_max_f32_e32 v12, 0xda24260, v12
	v_max_f32_e32 v6, 0xda24260, v6
	v_max_f32_e32 v0, 0xda24260, v0
	v_rcp_f32_e32 v12, v12
	v_rcp_f32_e32 v13, v6
	v_rcp_f32_e32 v6, v0
	v_and_b32_e32 v0, 0xffff0000, v7
	v_max_f32_e32 v0, v0, v0
	v_max_f32_e32 v0, 0xda24260, v0
	v_rcp_f32_e32 v7, v0
	v_pk_mul_f32 v[12:13], v[12:13], v[14:15]
	v_lshlrev_b32_e32 v14, 16, v2
	v_and_b32_e32 v15, 0xffff0000, v2
	v_lshlrev_b32_e32 v2, 16, v9
	v_max_f32_e32 v2, v2, v2
	v_lshlrev_b32_e32 v0, 16, v1
	v_and_b32_e32 v1, 0xffff0000, v1
	v_max_f32_e32 v2, 0xda24260, v2
	v_pk_mul_f32 v[0:1], v[6:7], v[0:1]
	v_lshlrev_b32_e32 v6, 16, v8
	v_and_b32_e32 v7, 0xffff0000, v8
	v_rcp_f32_e32 v8, v2
	v_and_b32_e32 v2, 0xffff0000, v9
	v_max_f32_e32 v6, v6, v6
	v_max_f32_e32 v7, v7, v7
	v_max_f32_e32 v2, v2, v2
	v_max_f32_e32 v6, 0xda24260, v6
	v_max_f32_e32 v7, 0xda24260, v7
	v_max_f32_e32 v2, 0xda24260, v2
	v_rcp_f32_e32 v6, v6
	v_rcp_f32_e32 v7, v7
	v_rcp_f32_e32 v9, v2
	v_lshlrev_b32_e32 v2, 16, v3
	v_and_b32_e32 v3, 0xffff0000, v3
	v_pk_mul_f32 v[6:7], v[6:7], v[14:15]
	v_pk_mul_f32 v[2:3], v[8:9], v[2:3]
	v_pk_mul_f32 v[80:81], v[80:81], v[0:1]
	v_pk_mul_f32 v[76:77], v[76:77], v[2:3]
	v_pk_mul_f32 v[74:75], v[74:75], v[6:7]
	s_waitcnt vmcnt(1)
	v_mov_b64_e32 v[0:1], v[44:45]
	v_mov_b64_e32 v[2:3], v[46:47]
	s_nop 0
	s_waitcnt vmcnt(0)
	v_mov_b64_e32 v[4:5], v[48:49]
	v_mov_b64_e32 v[6:7], v[50:51]
	v_pk_mul_f32 v[78:79], v[78:79], v[12:13]
	v_lshlrev_b32_e32 v10, 16, v0
	v_lshlrev_b32_e32 v8, 16, v4
	v_and_b32_e32 v4, 0xffff0000, v4
	v_and_b32_e32 v11, 0xffff0000, v0
	v_lshlrev_b32_e32 v0, 16, v5
	v_max_f32_e32 v8, v8, v8
	v_max_f32_e32 v4, v4, v4
	v_max_f32_e32 v0, v0, v0
	v_max_f32_e32 v8, 0xda24260, v8
	v_max_f32_e32 v4, 0xda24260, v4
	v_max_f32_e32 v0, 0xda24260, v0
	v_rcp_f32_e32 v8, v8
	v_rcp_f32_e32 v9, v4
	v_rcp_f32_e32 v4, v0
	v_and_b32_e32 v0, 0xffff0000, v5
	v_max_f32_e32 v0, v0, v0
	v_max_f32_e32 v0, 0xda24260, v0
	v_rcp_f32_e32 v5, v0
	v_pk_mul_f32 v[8:9], v[8:9], v[10:11]
	v_lshlrev_b32_e32 v10, 16, v2
	v_and_b32_e32 v11, 0xffff0000, v2
	v_lshlrev_b32_e32 v2, 16, v7
	v_max_f32_e32 v2, v2, v2
	v_lshlrev_b32_e32 v0, 16, v1
	v_and_b32_e32 v1, 0xffff0000, v1
	v_max_f32_e32 v2, 0xda24260, v2
	v_pk_mul_f32 v[0:1], v[4:5], v[0:1]
	v_lshlrev_b32_e32 v4, 16, v6
	v_and_b32_e32 v5, 0xffff0000, v6
	v_rcp_f32_e32 v6, v2
	v_and_b32_e32 v2, 0xffff0000, v7
	v_max_f32_e32 v4, v4, v4
	v_max_f32_e32 v5, v5, v5
	v_max_f32_e32 v2, v2, v2
	v_max_f32_e32 v4, 0xda24260, v4
	v_max_f32_e32 v5, 0xda24260, v5
	v_max_f32_e32 v2, 0xda24260, v2
	v_rcp_f32_e32 v4, v4
	v_rcp_f32_e32 v5, v5
	v_rcp_f32_e32 v7, v2
	v_lshlrev_b32_e32 v2, 16, v3
	v_and_b32_e32 v3, 0xffff0000, v3
	v_pk_mul_f32 v[4:5], v[4:5], v[10:11]
	v_pk_mul_f32 v[2:3], v[6:7], v[2:3]
	v_pk_mul_f32 v[72:73], v[72:73], v[0:1]
	v_pk_mul_f32 v[70:71], v[70:71], v[8:9]
	v_pk_mul_f32 v[68:69], v[68:69], v[2:3]
	v_pk_mul_f32 v[66:67], v[66:67], v[4:5]
